# attention epilogue: 31 serialized LDS exchange reads (read->lgkmcnt(0)->fma) issued in 3 batches into unused registers with counted waits; on top of the batched out-proj residual loads
# speedup vs baseline: 1.0069x; 1.0032x over previous
.LBB0_1136:
	s_or_b64 exec, exec, s[0:1]
	s_movk_i32 s0, 0x100
	v_cmp_gt_u32_e32 vcc, s0, v165
	s_waitcnt lgkmcnt(0)
	s_barrier
	s_and_saveexec_b64 s[12:13], vcc
	s_cbranch_execz .LBB0_1116
	v_lshlrev_b32_e32 v107, 8, v165
	v_lshl_add_u32 v106, v200, 2, 0
	v_and_b32_e32 v66, 0xc000, v107
	v_add_u32_e32 v108, v106, v66
	ds_read2st64_b32 v[136:137], v108 offset1:1
	ds_read2st64_b32 v[138:139], v108 offset0:2 offset1:3
	ds_read2st64_b32 v[140:141], v108 offset0:4 offset1:5
	ds_read2st64_b32 v[142:143], v108 offset0:6 offset1:7
	ds_read2st64_b32 v[144:145], v108 offset0:8 offset1:9
	ds_read2st64_b32 v[146:147], v108 offset0:10 offset1:11
	ds_read2st64_b32 v[148:149], v108 offset0:14 offset1:15
	ds_read2st64_b32 v[150:151], v108 offset0:12 offset1:13
	ds_read2st64_b32 v[152:153], v108 offset0:18 offset1:19
	ds_read2st64_b32 v[154:155], v108 offset0:16 offset1:17
	v_lshlrev_b32_e32 v162, 2, v175
	s_lshl_b64 s[0:1], s[6:7], 11
	v_readlane_b32 s2, v251, 35
	s_add_u32 s0, s2, s0
	s_waitcnt lgkmcnt(9)
	v_fma_f32 v73, v50, v105, -v136
	v_fma_f32 v72, v51, v104, -v137
	v_readlane_b32 s2, v251, 37
	s_addc_u32 s1, s2, s1
	s_lshl_b32 s2, s39, 8
	s_add_u32 s6, s0, s2
	s_waitcnt lgkmcnt(8)
	v_fma_f32 v71, v52, v101, -v138
	v_fma_f32 v70, v53, v99, -v139
	s_addc_u32 s7, s1, 0
	v_mov_b32_e32 v165, v163
	s_movk_i32 s0, 0x1000
	s_waitcnt lgkmcnt(7)
	v_fma_f32 v69, v54, v95, -v140
	v_fma_f32 v67, v55, v102, -v141
	s_waitcnt lgkmcnt(6)
	v_fma_f32 v68, v56, v98, -v142
	v_fma_f32 v66, v57, v96, -v143
	s_waitcnt lgkmcnt(5)
	v_fma_f32 v57, v58, v103, -v144
	v_fma_f32 v56, v59, v100, -v145
	s_waitcnt lgkmcnt(4)
	v_fma_f32 v55, v60, v97, -v146
	v_fma_f32 v54, v61, v94, -v147
	s_waitcnt lgkmcnt(3)
	v_fma_f32 v52, v64, v91, -v148
	s_waitcnt lgkmcnt(2)
	v_fma_f32 v53, v62, v93, -v150
	v_fma_f32 v50, v65, v90, -v149
	v_fma_f32 v51, v63, v92, -v151
	s_waitcnt lgkmcnt(0)
	v_fma_f32 v35, v35, v104, -v155
	s_waitcnt lgkmcnt(1)
	v_fma_f32 v59, v36, v101, -v152
	v_fma_f32 v36, v37, v99, -v153
	v_fma_f32 v58, v34, v105, -v154
	ds_read2st64_b32 v[136:137], v108 offset0:26 offset1:27
	ds_read2st64_b32 v[138:139], v108 offset0:20 offset1:21
	ds_read2st64_b32 v[140:141], v108 offset0:22 offset1:23
	ds_read2st64_b32 v[142:143], v108 offset0:24 offset1:25
	ds_read2st64_b32 v[144:145], v108 offset0:28 offset1:29
	ds_read2st64_b32 v[146:147], v108 offset0:30 offset1:31
	ds_read2st64_b32 v[148:149], v108 offset0:32 offset1:33
	ds_read2st64_b32 v[150:151], v108 offset0:34 offset1:35
	ds_read2st64_b32 v[152:153], v108 offset0:36 offset1:37
	ds_read2st64_b32 v[154:155], v108 offset0:38 offset1:39
	ds_read2st64_b32 v[156:157], v108 offset0:40 offset1:41
	ds_read2st64_b32 v[158:159], v108 offset0:42 offset1:43
	ds_read2st64_b32 v[160:161], v108 offset0:46 offset1:47
	ds_read2st64_b32 v[226:227], v108 offset0:44 offset1:45
	v_mul_f32_e32 v86, v58, v58
	v_fmac_f32_e32 v86, v73, v73
	v_mul_f32_e32 v82, v35, v35
	s_waitcnt lgkmcnt(12)
	v_fma_f32 v37, v38, v95, -v138
	v_fma_f32 v34, v39, v102, -v139
	v_fmac_f32_e32 v82, v72, v72
	v_mul_f32_e32 v83, v59, v59
	v_fmac_f32_e32 v83, v71, v71
	v_mul_f32_e32 v78, v36, v36
	s_waitcnt lgkmcnt(11)
	v_fma_f32 v61, v40, v98, -v140
	v_fma_f32 v60, v41, v96, -v141
	s_waitcnt lgkmcnt(13)
	v_fma_f32 v40, v45, v94, -v137
	v_fmac_f32_e32 v78, v70, v70
	v_mul_f32_e32 v80, v37, v37
	v_fmac_f32_e32 v80, v69, v69
	s_waitcnt lgkmcnt(10)
	v_fma_f32 v41, v42, v103, -v142
	v_fma_f32 v38, v43, v100, -v143
	v_fma_f32 v43, v44, v97, -v136
	v_mul_f32_e32 v74, v34, v34
	v_fmac_f32_e32 v74, v67, v67
	v_mul_f32_e32 v89, v61, v61
	v_fmac_f32_e32 v89, v68, v68
	s_waitcnt lgkmcnt(9)
	v_fma_f32 v42, v46, v93, -v144
	v_fma_f32 v39, v47, v92, -v145
	v_mul_f32_e32 v87, v60, v60
	v_fmac_f32_e32 v87, v66, v66
	v_mul_f32_e32 v84, v41, v41
	v_fmac_f32_e32 v84, v57, v57
	s_waitcnt lgkmcnt(8)
	v_fma_f32 v45, v48, v91, -v146
	v_fma_f32 v44, v49, v90, -v147
	v_mul_f32_e32 v79, v38, v38
	v_fmac_f32_e32 v79, v56, v56
	v_mul_f32_e32 v81, v43, v43
	v_fmac_f32_e32 v81, v55, v55
	s_waitcnt lgkmcnt(7)
	v_fma_f32 v76, v18, v105, -v148
	v_fma_f32 v63, v19, v104, -v149
	v_fmac_f32_e32 v86, v76, v76
	v_fmac_f32_e32 v82, v63, v63
	v_mul_f32_e32 v75, v40, v40
	v_fmac_f32_e32 v75, v54, v54
	s_waitcnt lgkmcnt(6)
	v_fma_f32 v65, v20, v101, -v150
	v_fma_f32 v62, v21, v99, -v151
	v_fmac_f32_e32 v83, v65, v65
	v_fmac_f32_e32 v78, v62, v62
	v_mul_f32_e32 v77, v42, v42
	v_fmac_f32_e32 v77, v53, v53
	s_waitcnt lgkmcnt(5)
	v_fma_f32 v49, v22, v95, -v152
	v_fma_f32 v48, v23, v102, -v153
	v_fmac_f32_e32 v80, v49, v49
	v_fmac_f32_e32 v74, v48, v48
	v_mul_f32_e32 v64, v39, v39
	v_fmac_f32_e32 v64, v51, v51
	s_waitcnt lgkmcnt(4)
	v_fma_f32 v47, v24, v98, -v154
	v_fma_f32 v46, v25, v96, -v155
	v_fmac_f32_e32 v89, v47, v47
	v_fmac_f32_e32 v87, v46, v46
	v_mul_f32_e32 v88, v45, v45
	v_fmac_f32_e32 v88, v52, v52
	s_waitcnt lgkmcnt(3)
	v_fma_f32 v25, v26, v103, -v156
	v_fma_f32 v24, v27, v100, -v157
	v_fmac_f32_e32 v84, v25, v25
	v_fmac_f32_e32 v79, v24, v24
	v_mul_f32_e32 v85, v44, v44
	s_waitcnt lgkmcnt(2)
	v_fma_f32 v23, v28, v97, -v158
	v_fma_f32 v22, v29, v94, -v159
	v_fmac_f32_e32 v81, v23, v23
	v_fmac_f32_e32 v75, v22, v22
	v_fmac_f32_e32 v85, v50, v50
	s_waitcnt lgkmcnt(0)
	v_fma_f32 v21, v30, v93, -v226
	v_fma_f32 v20, v31, v92, -v227
	s_waitcnt lgkmcnt(1)
	v_fma_f32 v19, v32, v91, -v160
	v_fma_f32 v18, v33, v90, -v161
	ds_read2st64_b32 v[136:137], v108 offset0:48 offset1:49
	ds_read2st64_b32 v[138:139], v108 offset0:50 offset1:51
	ds_read2st64_b32 v[140:141], v108 offset0:52 offset1:53
	ds_read2st64_b32 v[142:143], v108 offset0:54 offset1:55
	ds_read2st64_b32 v[144:145], v108 offset0:56 offset1:57
	ds_read2st64_b32 v[146:147], v108 offset0:58 offset1:59
	ds_read2st64_b32 v[148:149], v108 offset0:60 offset1:61
	v_fmac_f32_e32 v77, v21, v21
	v_fmac_f32_e32 v64, v20, v20
	v_fmac_f32_e32 v88, v19, v19
	v_fmac_f32_e32 v85, v18, v18
	s_waitcnt lgkmcnt(6)
	v_fma_f32 v33, v2, v105, -v136
	v_fma_f32 v32, v3, v104, -v137
	v_fmac_f32_e32 v86, v33, v33
	v_fmac_f32_e32 v82, v32, v32
	s_waitcnt lgkmcnt(5)
	v_fma_f32 v31, v4, v101, -v138
	v_fma_f32 v30, v5, v99, -v139
	v_fmac_f32_e32 v83, v31, v31
	v_fmac_f32_e32 v78, v30, v30
	s_waitcnt lgkmcnt(4)
	v_fma_f32 v29, v6, v95, -v140
	v_fma_f32 v28, v7, v102, -v141
	v_fmac_f32_e32 v80, v29, v29
	v_fmac_f32_e32 v74, v28, v28
	s_waitcnt lgkmcnt(3)
	v_fma_f32 v27, v8, v98, -v142
	v_fma_f32 v26, v9, v96, -v143
	v_fmac_f32_e32 v89, v27, v27
	v_fmac_f32_e32 v87, v26, v26
	s_waitcnt lgkmcnt(2)
	v_fma_f32 v9, v10, v103, -v144
	v_fma_f32 v8, v11, v100, -v145
	v_fmac_f32_e32 v84, v9, v9
	v_fmac_f32_e32 v79, v8, v8
	s_waitcnt lgkmcnt(1)
	v_fma_f32 v7, v12, v97, -v146
	v_fma_f32 v6, v13, v94, -v147
	v_fmac_f32_e32 v81, v7, v7
	v_fmac_f32_e32 v75, v6, v6
	s_waitcnt lgkmcnt(0)
	v_fma_f32 v5, v14, v93, -v148
	v_fma_f32 v4, v15, v92, -v149
	v_lshl_add_u64 v[14:15], s[48:49], 0, v[162:163]
	flat_load_dword v10, v[14:15]
	flat_load_dword v11, v[14:15] offset:128
	flat_load_dword v12, v[14:15] offset:256
	flat_load_dword v13, v[14:15] offset:384
	v_and_b32_e32 v15, 64, v189
	ds_read_b32 v2, v108 offset:15872
	v_xor_b32_e32 v14, 16, v189
	v_add_u32_e32 v15, 64, v15
	v_cmp_lt_i32_e32 vcc, v14, v15
	v_fmac_f32_e32 v77, v5, v5
	v_add_f32_dpp v15, v86, v86 quad_perm:[1,0,3,2] row_mask:0xf bank_mask:0xf bound_ctrl:1
	v_cndmask_b32_e32 v14, v189, v14, vcc
	v_lshlrev_b32_e32 v14, 2, v14
	v_add_f32_dpp v15, v15, v15 quad_perm:[2,3,0,1] row_mask:0xf bank_mask:0xf bound_ctrl:1
	s_waitcnt lgkmcnt(0)
	v_fma_f32 v3, v16, v91, -v2
	v_fmac_f32_e32 v64, v4, v4
	v_add_f32_dpp v15, v15, v15 row_half_mirror row_mask:0xf bank_mask:0xf bound_ctrl:1
	v_fmac_f32_e32 v88, v3, v3
	v_or_b32_e32 v2, 0x3f00, v107
	v_add_f32_dpp v15, v15, v15 row_mirror row_mask:0xf bank_mask:0xf bound_ctrl:1
	ds_bpermute_b32 v16, v14, v15
	v_add_u32_e32 v2, v106, v2
	ds_read_b32 v2, v2
	v_lshlrev_b32_e32 v162, 1, v175
	s_waitcnt lgkmcnt(0)
	v_add_f32_e32 v15, v15, v16
	v_fmamk_f32 v15, v15, 0x3c000000, v1
	v_rsq_f32_e32 v86, v15
	v_fma_f32 v2, v17, v90, -v2
	v_add_f32_dpp v15, v82, v82 quad_perm:[1,0,3,2] row_mask:0xf bank_mask:0xf bound_ctrl:1
	v_fmac_f32_e32 v85, v2, v2
	v_mov_b32_e32 v17, v163
	v_add_f32_dpp v15, v15, v15 quad_perm:[2,3,0,1] row_mask:0xf bank_mask:0xf bound_ctrl:1
	s_waitcnt vmcnt(0)
	v_mul_f32_e32 v10, v174, v10
	v_add_f32_dpp v15, v15, v15 row_half_mirror row_mask:0xf bank_mask:0xf bound_ctrl:1
	v_mul_f32_e32 v11, v174, v11
	v_mul_f32_e32 v12, v174, v12
	v_add_f32_dpp v15, v15, v15 row_mirror row_mask:0xf bank_mask:0xf bound_ctrl:1
	ds_bpermute_b32 v16, v14, v15
	v_mul_f32_e32 v13, v174, v13
	s_waitcnt lgkmcnt(0)
	v_add_f32_e32 v15, v15, v16
	v_fmamk_f32 v15, v15, 0x3c000000, v1
	v_rsq_f32_e32 v82, v15
	s_nop 0
	v_add_f32_dpp v15, v83, v83 quad_perm:[1,0,3,2] row_mask:0xf bank_mask:0xf bound_ctrl:1
	s_nop 1
	v_add_f32_dpp v15, v15, v15 quad_perm:[2,3,0,1] row_mask:0xf bank_mask:0xf bound_ctrl:1
	s_nop 1
	v_add_f32_dpp v15, v15, v15 row_half_mirror row_mask:0xf bank_mask:0xf bound_ctrl:1
	s_nop 1
	v_add_f32_dpp v15, v15, v15 row_mirror row_mask:0xf bank_mask:0xf bound_ctrl:1
	ds_bpermute_b32 v16, v14, v15
	s_waitcnt lgkmcnt(0)
	v_add_f32_e32 v15, v15, v16
	v_fmamk_f32 v15, v15, 0x3c000000, v1
	v_rsq_f32_e32 v83, v15
	s_nop 0
	v_add_f32_dpp v15, v78, v78 quad_perm:[1,0,3,2] row_mask:0xf bank_mask:0xf bound_ctrl:1
	v_mul_f32_e32 v31, v31, v83
	s_nop 0
	v_add_f32_dpp v15, v15, v15 quad_perm:[2,3,0,1] row_mask:0xf bank_mask:0xf bound_ctrl:1
	v_mul_f32_e32 v31, v13, v31
	v_add_u32_e32 v31, 0x8000, v31
	v_add_f32_dpp v15, v15, v15 row_half_mirror row_mask:0xf bank_mask:0xf bound_ctrl:1
	s_nop 1
	v_add_f32_dpp v15, v15, v15 row_mirror row_mask:0xf bank_mask:0xf bound_ctrl:1
	ds_bpermute_b32 v16, v14, v15
	s_waitcnt lgkmcnt(0)
	v_add_f32_e32 v15, v15, v16
	v_fmamk_f32 v15, v15, 0x3c000000, v1
	v_rsq_f32_e32 v78, v15
	s_nop 0
	v_add_f32_dpp v15, v80, v80 quad_perm:[1,0,3,2] row_mask:0xf bank_mask:0xf bound_ctrl:1
	v_mul_f32_e32 v30, v30, v78
	s_nop 0
	v_add_f32_dpp v15, v15, v15 quad_perm:[2,3,0,1] row_mask:0xf bank_mask:0xf bound_ctrl:1
	v_mul_f32_e32 v30, v13, v30
	v_add_u32_e32 v30, 0x8000, v30
	v_add_f32_dpp v15, v15, v15 row_half_mirror row_mask:0xf bank_mask:0xf bound_ctrl:1
	s_nop 1
	v_add_f32_dpp v15, v15, v15 row_mirror row_mask:0xf bank_mask:0xf bound_ctrl:1
	ds_bpermute_b32 v16, v14, v15
	s_waitcnt lgkmcnt(0)
	v_add_f32_e32 v15, v15, v16
	v_fmamk_f32 v15, v15, 0x3c000000, v1
	v_rsq_f32_e32 v80, v15
	s_nop 0
	v_add_f32_dpp v15, v74, v74 quad_perm:[1,0,3,2] row_mask:0xf bank_mask:0xf bound_ctrl:1
	v_mul_f32_e32 v29, v29, v80
	s_nop 0
	v_add_f32_dpp v15, v15, v15 quad_perm:[2,3,0,1] row_mask:0xf bank_mask:0xf bound_ctrl:1
	v_mul_f32_e32 v29, v13, v29
	v_add_u32_e32 v29, 0x8000, v29
	v_add_f32_dpp v15, v15, v15 row_half_mirror row_mask:0xf bank_mask:0xf bound_ctrl:1
	s_nop 1
	v_add_f32_dpp v15, v15, v15 row_mirror row_mask:0xf bank_mask:0xf bound_ctrl:1
	ds_bpermute_b32 v16, v14, v15
	s_waitcnt lgkmcnt(0)
	v_add_f32_e32 v15, v15, v16
	v_fmamk_f32 v15, v15, 0x3c000000, v1
	v_rsq_f32_e32 v74, v15
	s_nop 0
	v_add_f32_dpp v15, v89, v89 quad_perm:[1,0,3,2] row_mask:0xf bank_mask:0xf bound_ctrl:1
	v_mul_f32_e32 v28, v28, v74
	s_nop 0
	v_add_f32_dpp v15, v15, v15 quad_perm:[2,3,0,1] row_mask:0xf bank_mask:0xf bound_ctrl:1
	v_mul_f32_e32 v28, v13, v28
	v_add_u32_e32 v28, 0x8000, v28
	v_add_f32_dpp v15, v15, v15 row_half_mirror row_mask:0xf bank_mask:0xf bound_ctrl:1
	s_nop 1
	v_add_f32_dpp v15, v15, v15 row_mirror row_mask:0xf bank_mask:0xf bound_ctrl:1
	ds_bpermute_b32 v16, v14, v15
	s_waitcnt lgkmcnt(0)
	v_add_f32_e32 v15, v15, v16
	v_fmamk_f32 v15, v15, 0x3c000000, v1
	v_rsq_f32_e32 v89, v15
	s_nop 0
	v_add_f32_dpp v15, v87, v87 quad_perm:[1,0,3,2] row_mask:0xf bank_mask:0xf bound_ctrl:1
	s_nop 1
	v_add_f32_dpp v15, v15, v15 quad_perm:[2,3,0,1] row_mask:0xf bank_mask:0xf bound_ctrl:1
	s_nop 1
	v_add_f32_dpp v15, v15, v15 row_half_mirror row_mask:0xf bank_mask:0xf bound_ctrl:1
	s_nop 1
	v_add_f32_dpp v15, v15, v15 row_mirror row_mask:0xf bank_mask:0xf bound_ctrl:1
	ds_bpermute_b32 v16, v14, v15
	s_waitcnt lgkmcnt(0)
	v_add_f32_e32 v15, v15, v16
	v_fmamk_f32 v15, v15, 0x3c000000, v1
	v_rsq_f32_e32 v87, v15
	s_nop 0
	v_add_f32_dpp v15, v84, v84 quad_perm:[1,0,3,2] row_mask:0xf bank_mask:0xf bound_ctrl:1
	s_nop 1
	v_add_f32_dpp v15, v15, v15 quad_perm:[2,3,0,1] row_mask:0xf bank_mask:0xf bound_ctrl:1
	s_nop 1
	v_add_f32_dpp v15, v15, v15 row_half_mirror row_mask:0xf bank_mask:0xf bound_ctrl:1
	s_nop 1
	v_add_f32_dpp v15, v15, v15 row_mirror row_mask:0xf bank_mask:0xf bound_ctrl:1
	ds_bpermute_b32 v16, v14, v15
	s_waitcnt lgkmcnt(0)
	v_add_f32_e32 v15, v15, v16
	v_fmamk_f32 v15, v15, 0x3c000000, v1
	v_rsq_f32_e32 v84, v15
	s_nop 0
	v_add_f32_dpp v15, v79, v79 quad_perm:[1,0,3,2] row_mask:0xf bank_mask:0xf bound_ctrl:1
	v_mul_f32_e32 v9, v9, v84
	s_nop 0
	v_add_f32_dpp v15, v15, v15 quad_perm:[2,3,0,1] row_mask:0xf bank_mask:0xf bound_ctrl:1
	v_mul_f32_e32 v9, v13, v9
	v_add_u32_e32 v9, 0x8000, v9
	v_add_f32_dpp v15, v15, v15 row_half_mirror row_mask:0xf bank_mask:0xf bound_ctrl:1
	v_mul_f32_e32 v25, v25, v84
	v_mul_f32_e32 v25, v12, v25
	v_add_f32_dpp v15, v15, v15 row_mirror row_mask:0xf bank_mask:0xf bound_ctrl:1
	ds_bpermute_b32 v16, v14, v15
	v_add_u32_e32 v25, 0x8000, v25
	s_waitcnt lgkmcnt(0)
	v_add_f32_e32 v15, v15, v16
	v_fmamk_f32 v15, v15, 0x3c000000, v1
	v_rsq_f32_e32 v79, v15
	s_nop 0
	v_add_f32_dpp v15, v81, v81 quad_perm:[1,0,3,2] row_mask:0xf bank_mask:0xf bound_ctrl:1
	v_mul_f32_e32 v8, v8, v79
	s_nop 0
	v_add_f32_dpp v15, v15, v15 quad_perm:[2,3,0,1] row_mask:0xf bank_mask:0xf bound_ctrl:1
	v_mul_f32_e32 v8, v13, v8
	v_add_u32_e32 v8, 0x8000, v8
	v_add_f32_dpp v15, v15, v15 row_half_mirror row_mask:0xf bank_mask:0xf bound_ctrl:1
	s_nop 1
	v_add_f32_dpp v15, v15, v15 row_mirror row_mask:0xf bank_mask:0xf bound_ctrl:1
	ds_bpermute_b32 v16, v14, v15
	s_waitcnt lgkmcnt(0)
	v_add_f32_e32 v15, v15, v16
	v_fmamk_f32 v15, v15, 0x3c000000, v1
	v_rsq_f32_e32 v81, v15
	s_nop 0
	v_add_f32_dpp v15, v75, v75 quad_perm:[1,0,3,2] row_mask:0xf bank_mask:0xf bound_ctrl:1
	v_mul_f32_e32 v7, v7, v81
	s_nop 0
	v_add_f32_dpp v15, v15, v15 quad_perm:[2,3,0,1] row_mask:0xf bank_mask:0xf bound_ctrl:1
	v_mul_f32_e32 v7, v13, v7
	v_add_u32_e32 v7, 0x8000, v7
	v_add_f32_dpp v15, v15, v15 row_half_mirror row_mask:0xf bank_mask:0xf bound_ctrl:1
	s_nop 1
	v_add_f32_dpp v15, v15, v15 row_mirror row_mask:0xf bank_mask:0xf bound_ctrl:1
	ds_bpermute_b32 v16, v14, v15
	s_waitcnt lgkmcnt(0)
	v_add_f32_e32 v15, v15, v16
	v_fmamk_f32 v15, v15, 0x3c000000, v1
	v_rsq_f32_e32 v75, v15
	s_nop 0
	v_add_f32_dpp v15, v77, v77 quad_perm:[1,0,3,2] row_mask:0xf bank_mask:0xf bound_ctrl:1
	v_mul_f32_e32 v6, v6, v75
	s_nop 0
	v_add_f32_dpp v15, v15, v15 quad_perm:[2,3,0,1] row_mask:0xf bank_mask:0xf bound_ctrl:1
	v_mul_f32_e32 v6, v13, v6
	v_add_u32_e32 v6, 0x8000, v6
	v_add_f32_dpp v15, v15, v15 row_half_mirror row_mask:0xf bank_mask:0xf bound_ctrl:1
	s_nop 1
	v_add_f32_dpp v15, v15, v15 row_mirror row_mask:0xf bank_mask:0xf bound_ctrl:1
	ds_bpermute_b32 v16, v14, v15
	s_waitcnt lgkmcnt(0)
	v_add_f32_e32 v15, v15, v16
	v_fmamk_f32 v15, v15, 0x3c000000, v1
	v_rsq_f32_e32 v77, v15
	s_nop 0
	v_add_f32_dpp v15, v64, v64 quad_perm:[1,0,3,2] row_mask:0xf bank_mask:0xf bound_ctrl:1
	v_mul_f32_e32 v5, v5, v77
	s_nop 0
	v_add_f32_dpp v15, v15, v15 quad_perm:[2,3,0,1] row_mask:0xf bank_mask:0xf bound_ctrl:1
	v_mul_f32_e32 v5, v13, v5
	v_add_u32_e32 v5, 0x8000, v5
	v_add_f32_dpp v15, v15, v15 row_half_mirror row_mask:0xf bank_mask:0xf bound_ctrl:1
	s_nop 1
	v_add_f32_dpp v15, v15, v15 row_mirror row_mask:0xf bank_mask:0xf bound_ctrl:1
	ds_bpermute_b32 v16, v14, v15
	s_waitcnt lgkmcnt(0)
	v_add_f32_e32 v15, v15, v16
	v_fmamk_f32 v15, v15, 0x3c000000, v1
	v_rsq_f32_e32 v64, v15
	s_nop 0
	v_add_f32_dpp v15, v88, v88 quad_perm:[1,0,3,2] row_mask:0xf bank_mask:0xf bound_ctrl:1
	v_mul_f32_e32 v4, v4, v64
	s_nop 0
	v_add_f32_dpp v15, v15, v15 quad_perm:[2,3,0,1] row_mask:0xf bank_mask:0xf bound_ctrl:1
	v_mul_f32_e32 v4, v13, v4
	v_add_u32_e32 v4, 0x8000, v4
	v_add_f32_dpp v15, v15, v15 row_half_mirror row_mask:0xf bank_mask:0xf bound_ctrl:1
	s_nop 1
	v_add_f32_dpp v15, v15, v15 row_mirror row_mask:0xf bank_mask:0xf bound_ctrl:1
	ds_bpermute_b32 v16, v14, v15
	s_waitcnt lgkmcnt(0)
	v_add_f32_e32 v15, v15, v16
	v_fmamk_f32 v15, v15, 0x3c000000, v1
	v_rsq_f32_e32 v88, v15
	v_lshlrev_b32_e32 v16, 13, v176
	v_add_f32_dpp v15, v85, v85 quad_perm:[1,0,3,2] row_mask:0xf bank_mask:0xf bound_ctrl:1
	v_mul_f32_e32 v3, v3, v88
	s_nop 0
	v_add_f32_dpp v15, v15, v15 quad_perm:[2,3,0,1] row_mask:0xf bank_mask:0xf bound_ctrl:1
	v_mul_f32_e32 v3, v13, v3
	v_add_u32_e32 v3, 0x8000, v3
	v_add_f32_dpp v15, v15, v15 row_half_mirror row_mask:0xf bank_mask:0xf bound_ctrl:1
	s_nop 1
	v_add_f32_dpp v15, v15, v15 row_mirror row_mask:0xf bank_mask:0xf bound_ctrl:1
	ds_bpermute_b32 v14, v14, v15
	s_waitcnt lgkmcnt(0)
	v_add_f32_e32 v14, v15, v14
	v_fmamk_f32 v14, v14, 0x3c000000, v1
	v_rsq_f32_e32 v85, v14
	v_lshl_add_u64 v[14:15], s[6:7], 0, v[164:165]
	v_lshl_add_u64 v[14:15], v[14:15], 0, v[162:163]
	v_lshl_add_u64 v[14:15], v[14:15], 0, v[16:17]
	v_mul_f32_e32 v16, v73, v86
	v_mul_f32_e32 v16, v10, v16
	v_add_u32_e32 v16, 0x8000, v16
	global_store_short_d16_hi v[14:15], v16, off
	v_mul_f32_e32 v16, v58, v86
	v_mul_f32_e32 v16, v11, v16
	v_add_u32_e32 v16, 0x8000, v16
	global_store_short_d16_hi v[14:15], v16, off offset:64
	v_mul_f32_e32 v16, v76, v86
	v_mul_f32_e32 v16, v12, v16
	v_add_u32_e32 v16, 0x8000, v16
	global_store_short_d16_hi v[14:15], v16, off offset:128
	v_mul_f32_e32 v16, v33, v86
	v_mul_f32_e32 v16, v13, v16
	v_add_u32_e32 v16, 0x8000, v16
	global_store_short_d16_hi v[14:15], v16, off offset:192
	v_mul_f32_e32 v16, v72, v82
	v_mul_f32_e32 v16, v10, v16
	v_add_u32_e32 v16, 0x8000, v16
	global_store_short_d16_hi v[14:15], v16, off offset:2048
	v_mul_f32_e32 v16, v35, v82
	v_mul_f32_e32 v16, v11, v16
	v_add_u32_e32 v16, 0x8000, v16
	global_store_short_d16_hi v[14:15], v16, off offset:2112
	v_mul_f32_e32 v16, v63, v82
	v_mul_f32_e32 v16, v12, v16
	v_add_u32_e32 v16, 0x8000, v16
	global_store_short_d16_hi v[14:15], v16, off offset:2176
	v_mul_f32_e32 v16, v32, v82
	v_mul_f32_e32 v16, v13, v16
	v_add_u32_e32 v16, 0x8000, v16
	global_store_short_d16_hi v[14:15], v16, off offset:2240
	v_mul_f32_e32 v16, v71, v83
	v_mul_f32_e32 v16, v10, v16
	v_add_u32_e32 v32, 0x8000, v16
	v_add_co_u32_e32 v16, vcc, s0, v14
	s_movk_i32 s0, 0x5000
	s_nop 0
	v_addc_co_u32_e32 v17, vcc, 0, v15, vcc
	global_store_short_d16_hi v[16:17], v31, off offset:192
	v_mul_f32_e32 v31, v70, v78
	v_mul_f32_e32 v31, v10, v31
	v_add_u32_e32 v31, 0x8000, v31
	global_store_short_d16_hi v[16:17], v32, off
	v_mul_f32_e32 v32, v59, v83
	global_store_short_d16_hi v[16:17], v31, off offset:2048
	v_mul_f32_e32 v31, v36, v78
	v_mul_f32_e32 v32, v11, v32
	v_mul_f32_e32 v31, v11, v31
	v_add_u32_e32 v32, 0x8000, v32
	v_add_u32_e32 v31, 0x8000, v31
	global_store_short_d16_hi v[16:17], v32, off offset:64
	v_mul_f32_e32 v32, v65, v83
	global_store_short_d16_hi v[16:17], v31, off offset:2112
	v_mul_f32_e32 v31, v62, v78
	v_mul_f32_e32 v32, v12, v32
	v_mul_f32_e32 v31, v12, v31
	v_add_u32_e32 v32, 0x8000, v32
	v_add_u32_e32 v31, 0x8000, v31
	global_store_short_d16_hi v[16:17], v32, off offset:128
	global_store_short_d16_hi v[16:17], v31, off offset:2176
	global_store_short_d16_hi v[16:17], v30, off offset:2240
	v_mul_f32_e32 v16, v69, v80
	v_mul_f32_e32 v16, v10, v16
	v_add_u32_e32 v32, 0x8000, v16
	v_add_co_u32_e32 v16, vcc, s83, v14
	v_mul_f32_e32 v2, v2, v85
	s_nop 0
	v_addc_co_u32_e32 v17, vcc, 0, v15, vcc
	global_store_short_d16_hi v[16:17], v29, off offset:192
	v_mul_f32_e32 v29, v67, v74
	v_add_co_u32_e32 v30, vcc, s0, v14
	v_mul_f32_e32 v29, v10, v29
	s_nop 0
	v_addc_co_u32_e32 v31, vcc, 0, v15, vcc
	v_add_u32_e32 v29, 0x8000, v29
	global_store_short_d16_hi v[30:31], v32, off offset:-4096
	v_mul_f32_e32 v32, v37, v80
	global_store_short_d16_hi v[16:17], v29, off offset:2048
	v_mul_f32_e32 v29, v34, v74
	v_mul_f32_e32 v32, v11, v32
	v_mul_f32_e32 v29, v11, v29
	v_add_u32_e32 v32, 0x8000, v32
	v_add_u32_e32 v29, 0x8000, v29
	global_store_short_d16_hi v[16:17], v32, off offset:64
	v_mul_f32_e32 v32, v49, v80
	global_store_short_d16_hi v[16:17], v29, off offset:2112
	v_mul_f32_e32 v29, v48, v74
	v_mul_f32_e32 v32, v12, v32
	v_mul_f32_e32 v29, v12, v29
	v_add_u32_e32 v32, 0x8000, v32
	v_add_u32_e32 v29, 0x8000, v29
	global_store_short_d16_hi v[16:17], v32, off offset:128
	global_store_short_d16_hi v[16:17], v29, off offset:2176
	global_store_short_d16_hi v[16:17], v28, off offset:2240
	v_mul_f32_e32 v16, v68, v89
	v_mul_f32_e32 v16, v10, v16
	v_add_u32_e32 v16, 0x8000, v16
	global_store_short_d16_hi v[30:31], v16, off
	v_mul_f32_e32 v16, v61, v89
	v_mul_f32_e32 v16, v11, v16
	v_add_u32_e32 v16, 0x8000, v16
	global_store_short_d16_hi v[30:31], v16, off offset:64
	v_mul_f32_e32 v16, v47, v89
	v_mul_f32_e32 v16, v12, v16
	v_add_u32_e32 v16, 0x8000, v16
	global_store_short_d16_hi v[30:31], v16, off offset:128
	v_mul_f32_e32 v16, v27, v89
	v_mul_f32_e32 v16, v13, v16
	v_add_u32_e32 v16, 0x8000, v16
	global_store_short_d16_hi v[30:31], v16, off offset:192
	v_mul_f32_e32 v16, v66, v87
	v_mul_f32_e32 v16, v10, v16
	v_add_u32_e32 v16, 0x8000, v16
	global_store_short_d16_hi v[30:31], v16, off offset:2048
	v_mul_f32_e32 v16, v60, v87
	v_mul_f32_e32 v16, v11, v16
	v_add_u32_e32 v16, 0x8000, v16
	global_store_short_d16_hi v[30:31], v16, off offset:2112
	v_mul_f32_e32 v16, v46, v87
	v_mul_f32_e32 v16, v12, v16
	v_add_u32_e32 v16, 0x8000, v16
	global_store_short_d16_hi v[30:31], v16, off offset:2176
	v_mul_f32_e32 v16, v26, v87
	v_mul_f32_e32 v16, v13, v16
	v_add_u32_e32 v16, 0x8000, v16
	global_store_short_d16_hi v[30:31], v16, off offset:2240
	v_mul_f32_e32 v16, v57, v84
	v_mul_f32_e32 v16, v10, v16
	v_add_u32_e32 v28, 0x8000, v16
	v_add_co_u32_e32 v16, vcc, s90, v14
	s_mov_b32 s0, 0x9000
	s_nop 0
	v_addc_co_u32_e32 v17, vcc, 0, v15, vcc
	v_add_co_u32_e32 v26, vcc, s0, v14
	global_store_short_d16_hi v[16:17], v9, off offset:192
	s_nop 0
	v_addc_co_u32_e32 v27, vcc, 0, v15, vcc
	v_mul_f32_e32 v9, v56, v79
	v_mul_f32_e32 v9, v10, v9
	global_store_short_d16_hi v[26:27], v7, off offset:192
	v_mul_f32_e32 v7, v54, v75
	v_add_u32_e32 v9, 0x8000, v9
	global_store_short_d16_hi v[16:17], v8, off offset:2240
	v_mul_f32_e32 v8, v55, v81
	v_mul_f32_e32 v7, v10, v7
	global_store_short_d16_hi v[16:17], v9, off offset:2048
	v_mul_f32_e32 v9, v38, v79
	v_mul_f32_e32 v8, v10, v8
	v_add_u32_e32 v7, 0x8000, v7
	v_mul_f32_e32 v9, v11, v9
	v_add_u32_e32 v8, 0x8000, v8
	global_store_short_d16_hi v[26:27], v7, off offset:2048
	v_mul_f32_e32 v7, v40, v75
	v_add_u32_e32 v9, 0x8000, v9
	global_store_short_d16_hi v[26:27], v8, off
	v_mul_f32_e32 v8, v43, v81
	v_mul_f32_e32 v7, v11, v7
	global_store_short_d16_hi v[26:27], v28, off offset:-4096
	v_mul_f32_e32 v28, v41, v84
	global_store_short_d16_hi v[16:17], v9, off offset:2112
	v_mul_f32_e32 v9, v24, v79
	v_mul_f32_e32 v8, v11, v8
	v_add_u32_e32 v7, 0x8000, v7
	v_mul_f32_e32 v28, v11, v28
	v_mul_f32_e32 v9, v12, v9
	v_add_u32_e32 v8, 0x8000, v8
	global_store_short_d16_hi v[26:27], v7, off offset:2112
	v_mul_f32_e32 v7, v22, v75
	global_store_short_d16_hi v[26:27], v6, off offset:2240
	v_mul_f32_e32 v6, v53, v77
	v_add_u32_e32 v28, 0x8000, v28
	v_add_u32_e32 v9, 0x8000, v9
	global_store_short_d16_hi v[26:27], v8, off offset:64
	v_mul_f32_e32 v8, v23, v81
	v_mul_f32_e32 v7, v12, v7
	v_mul_f32_e32 v6, v10, v6
	global_store_short_d16_hi v[16:17], v28, off offset:64
	global_store_short_d16_hi v[16:17], v25, off offset:128
	global_store_short_d16_hi v[16:17], v9, off offset:2176
	v_mul_f32_e32 v8, v12, v8
	v_add_u32_e32 v7, 0x8000, v7
	v_add_u32_e32 v16, 0x8000, v6
	v_add_co_u32_e32 v6, vcc, s16, v14
	v_add_u32_e32 v8, 0x8000, v8
	global_store_short_d16_hi v[26:27], v7, off offset:2176
	v_addc_co_u32_e32 v7, vcc, 0, v15, vcc
	s_mov_b32 s0, 0xd000
	global_store_short_d16_hi v[26:27], v8, off offset:128
	v_add_co_u32_e32 v8, vcc, s0, v14
	global_store_short_d16_hi v[6:7], v5, off offset:192
	s_nop 0
	v_addc_co_u32_e32 v9, vcc, 0, v15, vcc
	v_mul_f32_e32 v5, v51, v64
	global_store_short_d16_hi v[6:7], v4, off offset:2240
	v_mul_f32_e32 v4, v52, v88
	global_store_short_d16_hi v[8:9], v3, off offset:192
	v_mul_f32_e32 v3, v50, v85
	v_mul_f32_e32 v5, v10, v5
	v_mul_f32_e32 v4, v10, v4
	v_mul_f32_e32 v3, v10, v3
	v_add_u32_e32 v5, 0x8000, v5
	v_add_u32_e32 v4, 0x8000, v4
	v_add_u32_e32 v3, 0x8000, v3
	v_mul_f32_e32 v14, v42, v77
	global_store_short_d16_hi v[6:7], v5, off offset:2048
	v_mul_f32_e32 v5, v39, v64
	global_store_short_d16_hi v[8:9], v4, off
	v_mul_f32_e32 v4, v45, v88
	global_store_short_d16_hi v[8:9], v3, off offset:2048
	v_mul_f32_e32 v3, v44, v85
	v_mul_f32_e32 v14, v11, v14
	v_mul_f32_e32 v5, v11, v5
	v_mul_f32_e32 v4, v11, v4
	v_mul_f32_e32 v3, v11, v3
	v_add_u32_e32 v14, 0x8000, v14
	v_add_u32_e32 v5, 0x8000, v5
	v_add_u32_e32 v4, 0x8000, v4
	v_add_u32_e32 v3, 0x8000, v3
	global_store_short_d16_hi v[6:7], v14, off offset:64
	v_mul_f32_e32 v14, v21, v77
	global_store_short_d16_hi v[6:7], v5, off offset:2112
	v_mul_f32_e32 v5, v20, v64
	global_store_short_d16_hi v[8:9], v4, off offset:64
	v_mul_f32_e32 v4, v19, v88
	global_store_short_d16_hi v[8:9], v3, off offset:2112
	v_mul_f32_e32 v3, v18, v85
	v_mul_f32_e32 v14, v12, v14
	v_mul_f32_e32 v5, v12, v5
	v_mul_f32_e32 v4, v12, v4
	v_mul_f32_e32 v3, v12, v3
	v_mul_f32_e32 v2, v13, v2
	v_add_u32_e32 v14, 0x8000, v14
	v_add_u32_e32 v5, 0x8000, v5
	v_add_u32_e32 v4, 0x8000, v4
	v_add_u32_e32 v3, 0x8000, v3
	v_add_u32_e32 v2, 0x8000, v2
	global_store_short_d16_hi v[8:9], v16, off offset:-4096
	global_store_short_d16_hi v[6:7], v14, off offset:128
	global_store_short_d16_hi v[6:7], v5, off offset:2176
	global_store_short_d16_hi v[8:9], v4, off offset:128
	global_store_short_d16_hi v[8:9], v3, off offset:2176
	global_store_short_d16_hi v[8:9], v2, off offset:2240
	s_branch .LBB0_1116
